# fast path for interior tiles in both attention layers, FoX bias folded into accumulator init
# speedup vs baseline: 1.0220x; 1.0071x over previous
.LBB0_556:
	s_cmp_le_i32 s63, s28
	s_cbranch_scc0 .Lorig_a0b0
	s_cmp_eq_u32 s17, 0
	s_cbranch_scc1 .Lorig_a0b0
	ds_read_b128 v[116:119], v189 offset:0
	ds_read_b128 v[120:123], v226 offset:0
	ds_read_b128 v[124:127], v227 offset:0
	ds_read_b128 v[128:131], v228 offset:0
	s_waitcnt lgkmcnt(3)
	v_mfma_f32_32x32x16_bf16 v[84:99], v[116:119], v[132:135], 0
	ds_read_b128 v[116:119], v232 offset:0
	s_waitcnt lgkmcnt(3)
	v_mfma_f32_32x32x16_bf16 v[84:99], v[120:123], v[136:139], v[84:99]
	ds_read_b128 v[120:123], v233 offset:0
	s_waitcnt lgkmcnt(3)
	v_mfma_f32_32x32x16_bf16 v[84:99], v[124:127], v[140:143], v[84:99]
	ds_read_b128 v[124:127], v234 offset:0
	s_waitcnt lgkmcnt(3)
	v_mfma_f32_32x32x16_bf16 v[84:99], v[128:131], v[144:147], v[84:99]
	ds_read_b128 v[128:131], v235 offset:0
	s_waitcnt lgkmcnt(3)
	v_mfma_f32_32x32x16_bf16 v[84:99], v[116:119], v[148:151], v[84:99]
	ds_read_b128 v[116:119], v190 offset:0
	s_waitcnt lgkmcnt(3)
	v_mfma_f32_32x32x16_bf16 v[84:99], v[120:123], v[152:155], v[84:99]
	ds_read_b128 v[120:123], v229 offset:0
	s_waitcnt lgkmcnt(3)
	v_mfma_f32_32x32x16_bf16 v[84:99], v[124:127], v[156:159], v[84:99]
	ds_read_b128 v[124:127], v230 offset:0
	s_waitcnt lgkmcnt(3)
	v_mfma_f32_32x32x16_bf16 v[84:99], v[128:131], v[160:163], v[84:99]
	ds_read_b128 v[128:131], v231 offset:0
	s_waitcnt lgkmcnt(3)
	v_mfma_f32_32x32x16_bf16 v[84:99], v[116:119], v[164:167], v[84:99]
	ds_read_b128 v[116:119], v189 offset:8192
	s_waitcnt lgkmcnt(3)
	v_mfma_f32_32x32x16_bf16 v[84:99], v[120:123], v[172:175], v[84:99]
	ds_read_b128 v[120:123], v226 offset:8192
	s_waitcnt lgkmcnt(3)
	v_mfma_f32_32x32x16_bf16 v[84:99], v[124:127], v[168:171], v[84:99]
	ds_read_b128 v[124:127], v227 offset:8192
	s_waitcnt lgkmcnt(3)
	v_mfma_f32_32x32x16_bf16 v[84:99], v[128:131], v[176:179], v[84:99]
	ds_read_b128 v[128:131], v228 offset:8192
	s_waitcnt lgkmcnt(3)
	v_mfma_f32_32x32x16_bf16 v[68:83], v[116:119], v[132:135], 0
	ds_read_b128 v[116:119], v232 offset:8192
	s_waitcnt lgkmcnt(3)
	v_mfma_f32_32x32x16_bf16 v[68:83], v[120:123], v[136:139], v[68:83]
	ds_read_b128 v[120:123], v233 offset:8192
	s_waitcnt lgkmcnt(3)
	v_mfma_f32_32x32x16_bf16 v[68:83], v[124:127], v[140:143], v[68:83]
	ds_read_b128 v[124:127], v234 offset:8192
	s_waitcnt lgkmcnt(3)
	v_mfma_f32_32x32x16_bf16 v[68:83], v[128:131], v[144:147], v[68:83]
	ds_read_b128 v[128:131], v235 offset:8192
	s_waitcnt lgkmcnt(3)
	v_mfma_f32_32x32x16_bf16 v[68:83], v[116:119], v[148:151], v[68:83]
	ds_read_b128 v[116:119], v190 offset:4096
	s_waitcnt lgkmcnt(3)
	v_mfma_f32_32x32x16_bf16 v[68:83], v[120:123], v[152:155], v[68:83]
	ds_read_b128 v[120:123], v229 offset:4096
	s_waitcnt lgkmcnt(3)
	v_mfma_f32_32x32x16_bf16 v[68:83], v[124:127], v[156:159], v[68:83]
	ds_read_b128 v[124:127], v230 offset:4096
	s_waitcnt lgkmcnt(3)
	v_mfma_f32_32x32x16_bf16 v[68:83], v[128:131], v[160:163], v[68:83]
	ds_read_b128 v[128:131], v231 offset:4096
	s_waitcnt lgkmcnt(3)
	v_mfma_f32_32x32x16_bf16 v[68:83], v[116:119], v[164:167], v[68:83]
	s_waitcnt lgkmcnt(2)
	v_mfma_f32_32x32x16_bf16 v[68:83], v[120:123], v[172:175], v[68:83]
	s_waitcnt lgkmcnt(1)
	v_mfma_f32_32x32x16_bf16 v[68:83], v[124:127], v[168:171], v[68:83]
	s_waitcnt lgkmcnt(0)
	v_mfma_f32_32x32x16_bf16 v[68:83], v[128:131], v[176:179], v[68:83]
	ds_read_b64_tr_b16 v[116:117], v191 offset:0
	ds_read_b64_tr_b16 v[118:119], v191 offset:2048
	ds_read_b64_tr_b16 v[120:121], v191 offset:4096
	ds_read_b64_tr_b16 v[122:123], v191 offset:6144
	ds_read_b64_tr_b16 v[124:125], v191 offset:8192
	ds_read_b64_tr_b16 v[126:127], v191 offset:10240
	ds_read_b64_tr_b16 v[128:129], v191 offset:12288
	ds_read_b64_tr_b16 v[130:131], v191 offset:14336
	s_nop 7
	s_nop 3
	v_cmp_eq_f32_e32 vcc, 0, v223
	s_cmp_eq_u64 vcc, exec
	s_cbranch_scc0 .Lsub_a0b0
	v_exp_f32_e32 v100, v84
	v_exp_f32_e32 v101, v85
	v_exp_f32_e32 v102, v86
	v_exp_f32_e32 v103, v87
	v_exp_f32_e32 v104, v88
	v_exp_f32_e32 v105, v89
	v_exp_f32_e32 v106, v90
	v_exp_f32_e32 v107, v91
	v_exp_f32_e32 v108, v92
	v_exp_f32_e32 v109, v93
	v_exp_f32_e32 v110, v94
	v_exp_f32_e32 v111, v95
	v_exp_f32_e32 v112, v96
	v_exp_f32_e32 v113, v97
	v_exp_f32_e32 v114, v98
	v_exp_f32_e32 v115, v99
	v_add_f32_e32 v237, v100, v101
	v_add_f32_e32 v251, v102, v103
	v_add_f32_e32 v237, v237, v104
	v_add_f32_e32 v251, v251, v105
	v_add_f32_e32 v237, v237, v106
	v_add_f32_e32 v251, v251, v107
	v_add_f32_e32 v237, v237, v108
	v_add_f32_e32 v251, v251, v109
	v_add_f32_e32 v237, v237, v110
	v_add_f32_e32 v251, v251, v111
	v_add_f32_e32 v237, v237, v112
	v_add_f32_e32 v251, v251, v113
	v_add_f32_e32 v237, v237, v114
	v_add_f32_e32 v251, v251, v115
	v_add_f32_e32 v237, v237, v251
	v_cvt_pk_bf16_f32 v238, v100, v101
	v_cvt_pk_bf16_f32 v239, v102, v103
	v_cvt_pk_bf16_f32 v240, v104, v105
	v_cvt_pk_bf16_f32 v241, v106, v107
	v_cvt_pk_bf16_f32 v242, v108, v109
	v_cvt_pk_bf16_f32 v243, v110, v111
	v_cvt_pk_bf16_f32 v244, v112, v113
	v_cvt_pk_bf16_f32 v245, v114, v115
	s_nop 1
	v_permlane32_swap_b32_e32 v238, v240
	v_permlane32_swap_b32_e32 v239, v241
	v_permlane32_swap_b32_e32 v242, v244
	v_permlane32_swap_b32_e32 v243, v245
	v_exp_f32_e32 v100, v68
	v_exp_f32_e32 v101, v69
	v_exp_f32_e32 v102, v70
	v_exp_f32_e32 v103, v71
	v_exp_f32_e32 v104, v72
	v_exp_f32_e32 v105, v73
	v_exp_f32_e32 v106, v74
	v_exp_f32_e32 v107, v75
	v_exp_f32_e32 v108, v76
	v_exp_f32_e32 v109, v77
	v_exp_f32_e32 v110, v78
	v_exp_f32_e32 v111, v79
	v_exp_f32_e32 v112, v80
	v_exp_f32_e32 v113, v81
	v_exp_f32_e32 v114, v82
	v_exp_f32_e32 v115, v83
	v_add_f32_e32 v250, v100, v101
	v_add_f32_e32 v251, v102, v103
	v_add_f32_e32 v250, v250, v104
	v_add_f32_e32 v251, v251, v105
	v_add_f32_e32 v250, v250, v106
	v_add_f32_e32 v251, v251, v107
	v_add_f32_e32 v250, v250, v108
	v_add_f32_e32 v251, v251, v109
	v_add_f32_e32 v250, v250, v110
	v_add_f32_e32 v251, v251, v111
	v_add_f32_e32 v250, v250, v112
	v_add_f32_e32 v251, v251, v113
	v_add_f32_e32 v250, v250, v114
	v_add_f32_e32 v251, v251, v115
	v_add_f32_e32 v250, v250, v251
	v_cvt_pk_bf16_f32 v100, v100, v101
	v_cvt_pk_bf16_f32 v101, v102, v103
	v_cvt_pk_bf16_f32 v102, v104, v105
	v_cvt_pk_bf16_f32 v103, v106, v107
	v_cvt_pk_bf16_f32 v104, v108, v109
	v_cvt_pk_bf16_f32 v105, v110, v111
	v_cvt_pk_bf16_f32 v106, v112, v113
	v_cvt_pk_bf16_f32 v107, v114, v115
	s_nop 1
	v_permlane32_swap_b32_e32 v100, v102
	v_permlane32_swap_b32_e32 v101, v103
	v_permlane32_swap_b32_e32 v104, v106
	v_permlane32_swap_b32_e32 v105, v107
	s_branch .Lsum_a0b0
.Lsub_a0b0:
	v_sub_f32_e32 v100, v84, v223
	v_sub_f32_e32 v101, v85, v223
	v_sub_f32_e32 v102, v86, v223
	v_sub_f32_e32 v103, v87, v223
	v_sub_f32_e32 v104, v88, v223
	v_sub_f32_e32 v105, v89, v223
	v_sub_f32_e32 v106, v90, v223
	v_sub_f32_e32 v107, v91, v223
	v_sub_f32_e32 v108, v92, v223
	v_sub_f32_e32 v109, v93, v223
	v_sub_f32_e32 v110, v94, v223
	v_sub_f32_e32 v111, v95, v223
	v_sub_f32_e32 v112, v96, v223
	v_sub_f32_e32 v113, v97, v223
	v_sub_f32_e32 v114, v98, v223
	v_sub_f32_e32 v115, v99, v223
	v_exp_f32_e32 v100, v100
	v_exp_f32_e32 v101, v101
	v_exp_f32_e32 v102, v102
	v_exp_f32_e32 v103, v103
	v_exp_f32_e32 v104, v104
	v_exp_f32_e32 v105, v105
	v_exp_f32_e32 v106, v106
	v_exp_f32_e32 v107, v107
	v_exp_f32_e32 v108, v108
	v_exp_f32_e32 v109, v109
	v_exp_f32_e32 v110, v110
	v_exp_f32_e32 v111, v111
	v_exp_f32_e32 v112, v112
	v_exp_f32_e32 v113, v113
	v_exp_f32_e32 v114, v114
	v_exp_f32_e32 v115, v115
	v_add_f32_e32 v237, v100, v101
	v_add_f32_e32 v251, v102, v103
	v_add_f32_e32 v237, v237, v104
	v_add_f32_e32 v251, v251, v105
	v_add_f32_e32 v237, v237, v106
	v_add_f32_e32 v251, v251, v107
	v_add_f32_e32 v237, v237, v108
	v_add_f32_e32 v251, v251, v109
	v_add_f32_e32 v237, v237, v110
	v_add_f32_e32 v251, v251, v111
	v_add_f32_e32 v237, v237, v112
	v_add_f32_e32 v251, v251, v113
	v_add_f32_e32 v237, v237, v114
	v_add_f32_e32 v251, v251, v115
	v_add_f32_e32 v237, v237, v251
	v_cvt_pk_bf16_f32 v238, v100, v101
	v_cvt_pk_bf16_f32 v239, v102, v103
	v_cvt_pk_bf16_f32 v240, v104, v105
	v_cvt_pk_bf16_f32 v241, v106, v107
	v_cvt_pk_bf16_f32 v242, v108, v109
	v_cvt_pk_bf16_f32 v243, v110, v111
	v_cvt_pk_bf16_f32 v244, v112, v113
	v_cvt_pk_bf16_f32 v245, v114, v115
	s_nop 1
	v_permlane32_swap_b32_e32 v238, v240
	v_permlane32_swap_b32_e32 v239, v241
	v_permlane32_swap_b32_e32 v242, v244
	v_permlane32_swap_b32_e32 v243, v245
	v_sub_f32_e32 v100, v68, v223
	v_sub_f32_e32 v101, v69, v223
	v_sub_f32_e32 v102, v70, v223
	v_sub_f32_e32 v103, v71, v223
	v_sub_f32_e32 v104, v72, v223
	v_sub_f32_e32 v105, v73, v223
	v_sub_f32_e32 v106, v74, v223
	v_sub_f32_e32 v107, v75, v223
	v_sub_f32_e32 v108, v76, v223
	v_sub_f32_e32 v109, v77, v223
	v_sub_f32_e32 v110, v78, v223
	v_sub_f32_e32 v111, v79, v223
	v_sub_f32_e32 v112, v80, v223
	v_sub_f32_e32 v113, v81, v223
	v_sub_f32_e32 v114, v82, v223
	v_sub_f32_e32 v115, v83, v223
	v_exp_f32_e32 v100, v100
	v_exp_f32_e32 v101, v101
	v_exp_f32_e32 v102, v102
	v_exp_f32_e32 v103, v103
	v_exp_f32_e32 v104, v104
	v_exp_f32_e32 v105, v105
	v_exp_f32_e32 v106, v106
	v_exp_f32_e32 v107, v107
	v_exp_f32_e32 v108, v108
	v_exp_f32_e32 v109, v109
	v_exp_f32_e32 v110, v110
	v_exp_f32_e32 v111, v111
	v_exp_f32_e32 v112, v112
	v_exp_f32_e32 v113, v113
	v_exp_f32_e32 v114, v114
	v_exp_f32_e32 v115, v115
	v_add_f32_e32 v250, v100, v101
	v_add_f32_e32 v251, v102, v103
	v_add_f32_e32 v250, v250, v104
	v_add_f32_e32 v251, v251, v105
	v_add_f32_e32 v250, v250, v106
	v_add_f32_e32 v251, v251, v107
	v_add_f32_e32 v250, v250, v108
	v_add_f32_e32 v251, v251, v109
	v_add_f32_e32 v250, v250, v110
	v_add_f32_e32 v251, v251, v111
	v_add_f32_e32 v250, v250, v112
	v_add_f32_e32 v251, v251, v113
	v_add_f32_e32 v250, v250, v114
	v_add_f32_e32 v251, v251, v115
	v_add_f32_e32 v250, v250, v251
	v_cvt_pk_bf16_f32 v100, v100, v101
	v_cvt_pk_bf16_f32 v101, v102, v103
	v_cvt_pk_bf16_f32 v102, v104, v105
	v_cvt_pk_bf16_f32 v103, v106, v107
	v_cvt_pk_bf16_f32 v104, v108, v109
	v_cvt_pk_bf16_f32 v105, v110, v111
	v_cvt_pk_bf16_f32 v106, v112, v113
	v_cvt_pk_bf16_f32 v107, v114, v115
	s_nop 1
	v_permlane32_swap_b32_e32 v100, v102
	v_permlane32_swap_b32_e32 v101, v103
	v_permlane32_swap_b32_e32 v104, v106
	v_permlane32_swap_b32_e32 v105, v107
.Lsum_a0b0:
	v_add_f32_e32 v237, v237, v250
	v_cmp_gt_f32_e32 vcc, 0x5f800000, v237
	s_cmp_eq_u64 vcc, exec
	s_cbranch_scc0 .Lfb_a0b0
	v_mov_b32_e32 v250, v237
	s_nop 1
	v_permlane32_swap_b32_e32 v237, v250
	v_add_f32_e32 v237, v237, v250
	v_add_f32_e32 v221, v237, v221
	v_mov_b32_e32 v222, v223
	s_waitcnt lgkmcnt(6)
	v_mfma_f32_32x32x16_bf16 v[52:67], v[116:119], v[238:241], v[52:67]
	ds_read_b64_tr_b16 v[116:117], v191 offset:512
	ds_read_b64_tr_b16 v[118:119], v191 offset:2560
	s_waitcnt lgkmcnt(6)
	v_mfma_f32_32x32x16_bf16 v[52:67], v[120:123], v[242:245], v[52:67]
	ds_read_b64_tr_b16 v[120:121], v191 offset:4608
	ds_read_b64_tr_b16 v[122:123], v191 offset:6656
	s_waitcnt lgkmcnt(6)
	v_mfma_f32_32x32x16_bf16 v[52:67], v[124:127], v[100:103], v[52:67]
	ds_read_b64_tr_b16 v[124:125], v191 offset:8704
	ds_read_b64_tr_b16 v[126:127], v191 offset:10752
	s_waitcnt lgkmcnt(6)
	v_mfma_f32_32x32x16_bf16 v[52:67], v[128:131], v[104:107], v[52:67]
	ds_read_b64_tr_b16 v[128:129], v191 offset:12800
	ds_read_b64_tr_b16 v[130:131], v191 offset:14848
	s_waitcnt lgkmcnt(6)
	v_mfma_f32_32x32x16_bf16 v[36:51], v[116:119], v[238:241], v[36:51]
	ds_read_b64_tr_b16 v[116:117], v191 offset:1024
	ds_read_b64_tr_b16 v[118:119], v191 offset:3072
	s_waitcnt lgkmcnt(6)
	v_mfma_f32_32x32x16_bf16 v[36:51], v[120:123], v[242:245], v[36:51]
	ds_read_b64_tr_b16 v[120:121], v191 offset:5120
	ds_read_b64_tr_b16 v[122:123], v191 offset:7168
	s_waitcnt lgkmcnt(6)
	v_mfma_f32_32x32x16_bf16 v[36:51], v[124:127], v[100:103], v[36:51]
	ds_read_b64_tr_b16 v[124:125], v191 offset:9216
	ds_read_b64_tr_b16 v[126:127], v191 offset:11264
	s_waitcnt lgkmcnt(6)
	v_mfma_f32_32x32x16_bf16 v[36:51], v[128:131], v[104:107], v[36:51]
	ds_read_b64_tr_b16 v[128:129], v191 offset:13312
	ds_read_b64_tr_b16 v[130:131], v191 offset:15360
	s_waitcnt lgkmcnt(6)
	v_mfma_f32_32x32x16_bf16 v[20:35], v[116:119], v[238:241], v[20:35]
	ds_read_b64_tr_b16 v[116:117], v191 offset:1536
	ds_read_b64_tr_b16 v[118:119], v191 offset:3584
	s_waitcnt lgkmcnt(6)
	v_mfma_f32_32x32x16_bf16 v[20:35], v[120:123], v[242:245], v[20:35]
	ds_read_b64_tr_b16 v[120:121], v191 offset:5632
	ds_read_b64_tr_b16 v[122:123], v191 offset:7680
	s_waitcnt lgkmcnt(6)
	v_mfma_f32_32x32x16_bf16 v[20:35], v[124:127], v[100:103], v[20:35]
	ds_read_b64_tr_b16 v[124:125], v191 offset:9728
	ds_read_b64_tr_b16 v[126:127], v191 offset:11776
	s_waitcnt lgkmcnt(6)
	v_mfma_f32_32x32x16_bf16 v[20:35], v[128:131], v[104:107], v[20:35]
	ds_read_b64_tr_b16 v[128:129], v191 offset:13824
	ds_read_b64_tr_b16 v[130:131], v191 offset:15872
	s_waitcnt lgkmcnt(6)
	v_mfma_f32_32x32x16_bf16 v[4:19], v[116:119], v[238:241], v[4:19]
	s_waitcnt lgkmcnt(4)
	v_mfma_f32_32x32x16_bf16 v[4:19], v[120:123], v[242:245], v[4:19]
	s_waitcnt lgkmcnt(2)
	v_mfma_f32_32x32x16_bf16 v[4:19], v[124:127], v[100:103], v[4:19]
	s_waitcnt lgkmcnt(0)
	v_mfma_f32_32x32x16_bf16 v[4:19], v[128:131], v[104:107], v[4:19]
	s_setprio 0
	s_branch .Ltail2_a0b0

.LBB0_564:
	v_add_f32_e32 v100, v84, v85
	ds_read_b64_tr_b16 v[84:85], v191 offset:0
	ds_read_b64_tr_b16 v[86:87], v191 offset:0x800
	ds_read_b64_tr_b16 v[88:89], v191 offset:0x1000
	ds_read_b64_tr_b16 v[90:91], v191 offset:0x1800
	ds_read_b64_tr_b16 v[92:93], v191 offset:0x2000
	ds_read_b64_tr_b16 v[94:95], v191 offset:0x2800
	ds_read_b64_tr_b16 v[96:97], v191 offset:0x3000
	ds_read_b64_tr_b16 v[98:99], v191 offset:0x3800
	v_fmac_f32_e32 v100, v221, v2
	s_waitcnt lgkmcnt(6)
	v_mfma_f32_32x32x16_bf16 v[52:67], v[84:87], v[68:71], v[52:67]
	ds_read_b64_tr_b16 v[84:85], v191 offset:0x200
	ds_read_b64_tr_b16 v[86:87], v191 offset:0xa00
	s_waitcnt lgkmcnt(6)
	v_mfma_f32_32x32x16_bf16 v[52:67], v[88:91], v[72:75], v[52:67]
	ds_read_b64_tr_b16 v[88:89], v191 offset:0x1200
	ds_read_b64_tr_b16 v[90:91], v191 offset:0x1a00
	s_waitcnt lgkmcnt(6)
	v_mfma_f32_32x32x16_bf16 v[52:67], v[92:95], v[76:79], v[52:67]
	ds_read_b64_tr_b16 v[92:93], v191 offset:0x2200
	ds_read_b64_tr_b16 v[94:95], v191 offset:0x2a00
	s_waitcnt lgkmcnt(6)
	v_mfma_f32_32x32x16_bf16 v[52:67], v[96:99], v[80:83], v[52:67]
	ds_read_b64_tr_b16 v[96:97], v191 offset:0x3200
	ds_read_b64_tr_b16 v[98:99], v191 offset:0x3a00
	s_waitcnt lgkmcnt(6)
	v_mfma_f32_32x32x16_bf16 v[36:51], v[84:87], v[68:71], v[36:51]
	ds_read_b64_tr_b16 v[84:85], v191 offset:0x400
	ds_read_b64_tr_b16 v[86:87], v191 offset:0xc00
	s_waitcnt lgkmcnt(6)
	v_mfma_f32_32x32x16_bf16 v[36:51], v[88:91], v[72:75], v[36:51]
	ds_read_b64_tr_b16 v[88:89], v191 offset:0x1400
	ds_read_b64_tr_b16 v[90:91], v191 offset:0x1c00
	s_waitcnt lgkmcnt(6)
	v_mfma_f32_32x32x16_bf16 v[36:51], v[92:95], v[76:79], v[36:51]
	ds_read_b64_tr_b16 v[92:93], v191 offset:0x2400
	ds_read_b64_tr_b16 v[94:95], v191 offset:0x2c00
	s_waitcnt lgkmcnt(6)
	v_mfma_f32_32x32x16_bf16 v[36:51], v[96:99], v[80:83], v[36:51]
	ds_read_b64_tr_b16 v[96:97], v191 offset:0x3400
	ds_read_b64_tr_b16 v[98:99], v191 offset:0x3c00
	s_waitcnt lgkmcnt(6)
	v_mfma_f32_32x32x16_bf16 v[20:35], v[84:87], v[68:71], v[20:35]
	ds_read_b64_tr_b16 v[84:85], v191 offset:0x600
	ds_read_b64_tr_b16 v[86:87], v191 offset:0xe00
	s_waitcnt lgkmcnt(6)
	v_mfma_f32_32x32x16_bf16 v[20:35], v[88:91], v[72:75], v[20:35]
	ds_read_b64_tr_b16 v[88:89], v191 offset:0x1600
	ds_read_b64_tr_b16 v[90:91], v191 offset:0x1e00
	s_waitcnt lgkmcnt(6)
	v_mfma_f32_32x32x16_bf16 v[20:35], v[92:95], v[76:79], v[20:35]
	ds_read_b64_tr_b16 v[92:93], v191 offset:0x2600
	ds_read_b64_tr_b16 v[94:95], v191 offset:0x2e00
	s_waitcnt lgkmcnt(6)
	v_mfma_f32_32x32x16_bf16 v[20:35], v[96:99], v[80:83], v[20:35]
	ds_read_b64_tr_b16 v[96:97], v191 offset:0x3600
	ds_read_b64_tr_b16 v[98:99], v191 offset:0x3e00
	s_waitcnt lgkmcnt(6)
	v_mfma_f32_32x32x16_bf16 v[4:19], v[84:87], v[68:71], v[4:19]
	s_waitcnt lgkmcnt(4)
	v_mfma_f32_32x32x16_bf16 v[4:19], v[88:91], v[72:75], v[4:19]
	s_waitcnt lgkmcnt(2)
	v_mfma_f32_32x32x16_bf16 v[4:19], v[92:95], v[76:79], v[4:19]
	s_waitcnt lgkmcnt(0)
	v_mfma_f32_32x32x16_bf16 v[4:19], v[96:99], v[80:83], v[4:19]
	s_setprio 0
	v_mov_b32_e32 v221, v100
.Ltail2_a0b0:
	s_and_b64 vcc, exec, s[4:5]
	s_cbranch_vccz .LBB0_543
	s_branch .LBB0_544

.LBB0_571:
	s_add_i32 s98, s63, 64
	s_cmp_le_i32 s98, s28
	s_cbranch_scc0 .Lorig_a0b1
	ds_read_b128 v[116:119], v189 offset:24576
	ds_read_b128 v[120:123], v226 offset:24576
	ds_read_b128 v[124:127], v227 offset:24576
	ds_read_b128 v[128:131], v228 offset:24576
	s_waitcnt lgkmcnt(3)
	v_mfma_f32_32x32x16_bf16 v[84:99], v[116:119], v[132:135], 0
	ds_read_b128 v[116:119], v232 offset:24576
	s_waitcnt lgkmcnt(3)
	v_mfma_f32_32x32x16_bf16 v[84:99], v[120:123], v[136:139], v[84:99]
	ds_read_b128 v[120:123], v233 offset:24576
	s_waitcnt lgkmcnt(3)
	v_mfma_f32_32x32x16_bf16 v[84:99], v[124:127], v[140:143], v[84:99]
	ds_read_b128 v[124:127], v234 offset:24576
	s_waitcnt lgkmcnt(3)
	v_mfma_f32_32x32x16_bf16 v[84:99], v[128:131], v[144:147], v[84:99]
	ds_read_b128 v[128:131], v235 offset:24576
	s_waitcnt lgkmcnt(3)
	v_mfma_f32_32x32x16_bf16 v[84:99], v[116:119], v[148:151], v[84:99]
	ds_read_b128 v[116:119], v190 offset:24576
	s_waitcnt lgkmcnt(3)
	v_mfma_f32_32x32x16_bf16 v[84:99], v[120:123], v[152:155], v[84:99]
	ds_read_b128 v[120:123], v229 offset:24576
	s_waitcnt lgkmcnt(3)
	v_mfma_f32_32x32x16_bf16 v[84:99], v[124:127], v[156:159], v[84:99]
	ds_read_b128 v[124:127], v230 offset:24576
	s_waitcnt lgkmcnt(3)
	v_mfma_f32_32x32x16_bf16 v[84:99], v[128:131], v[160:163], v[84:99]
	ds_read_b128 v[128:131], v231 offset:24576
	s_waitcnt lgkmcnt(3)
	v_mfma_f32_32x32x16_bf16 v[84:99], v[116:119], v[164:167], v[84:99]
	ds_read_b128 v[116:119], v189 offset:32768
	s_waitcnt lgkmcnt(3)
	v_mfma_f32_32x32x16_bf16 v[84:99], v[120:123], v[172:175], v[84:99]
	ds_read_b128 v[120:123], v226 offset:32768
	s_waitcnt lgkmcnt(3)
	v_mfma_f32_32x32x16_bf16 v[84:99], v[124:127], v[168:171], v[84:99]
	ds_read_b128 v[124:127], v227 offset:32768
	s_waitcnt lgkmcnt(3)
	v_mfma_f32_32x32x16_bf16 v[84:99], v[128:131], v[176:179], v[84:99]
	ds_read_b128 v[128:131], v228 offset:32768
	s_waitcnt lgkmcnt(3)
	v_mfma_f32_32x32x16_bf16 v[68:83], v[116:119], v[132:135], 0
	ds_read_b128 v[116:119], v232 offset:32768
	s_waitcnt lgkmcnt(3)
	v_mfma_f32_32x32x16_bf16 v[68:83], v[120:123], v[136:139], v[68:83]
	ds_read_b128 v[120:123], v233 offset:32768
	s_waitcnt lgkmcnt(3)
	v_mfma_f32_32x32x16_bf16 v[68:83], v[124:127], v[140:143], v[68:83]
	ds_read_b128 v[124:127], v234 offset:32768
	s_waitcnt lgkmcnt(3)
	v_mfma_f32_32x32x16_bf16 v[68:83], v[128:131], v[144:147], v[68:83]
	ds_read_b128 v[128:131], v235 offset:32768
	s_waitcnt lgkmcnt(3)
	v_mfma_f32_32x32x16_bf16 v[68:83], v[116:119], v[148:151], v[68:83]
	ds_read_b128 v[116:119], v190 offset:28672
	s_waitcnt lgkmcnt(3)
	v_mfma_f32_32x32x16_bf16 v[68:83], v[120:123], v[152:155], v[68:83]
	ds_read_b128 v[120:123], v229 offset:28672
	s_waitcnt lgkmcnt(3)
	v_mfma_f32_32x32x16_bf16 v[68:83], v[124:127], v[156:159], v[68:83]
	ds_read_b128 v[124:127], v230 offset:28672
	s_waitcnt lgkmcnt(3)
	v_mfma_f32_32x32x16_bf16 v[68:83], v[128:131], v[160:163], v[68:83]
	ds_read_b128 v[128:131], v231 offset:28672
	s_waitcnt lgkmcnt(3)
	v_mfma_f32_32x32x16_bf16 v[68:83], v[116:119], v[164:167], v[68:83]
	s_waitcnt lgkmcnt(2)
	v_mfma_f32_32x32x16_bf16 v[68:83], v[120:123], v[172:175], v[68:83]
	s_waitcnt lgkmcnt(1)
	v_mfma_f32_32x32x16_bf16 v[68:83], v[124:127], v[168:171], v[68:83]
	s_waitcnt lgkmcnt(0)
	v_mfma_f32_32x32x16_bf16 v[68:83], v[128:131], v[176:179], v[68:83]
	ds_read_b64_tr_b16 v[116:117], v191 offset:16384
	ds_read_b64_tr_b16 v[118:119], v191 offset:18432
	ds_read_b64_tr_b16 v[120:121], v191 offset:20480
	ds_read_b64_tr_b16 v[122:123], v191 offset:22528
	ds_read_b64_tr_b16 v[124:125], v191 offset:24576
	ds_read_b64_tr_b16 v[126:127], v191 offset:26624
	ds_read_b64_tr_b16 v[128:129], v191 offset:28672
	ds_read_b64_tr_b16 v[130:131], v191 offset:30720
	s_nop 7
	s_nop 3
	v_cmp_eq_f32_e32 vcc, 0, v222
	s_cmp_eq_u64 vcc, exec
	s_cbranch_scc0 .Lsub_a0b1
	v_exp_f32_e32 v100, v84
	v_exp_f32_e32 v101, v85
	v_exp_f32_e32 v102, v86
	v_exp_f32_e32 v103, v87
	v_exp_f32_e32 v104, v88
	v_exp_f32_e32 v105, v89
	v_exp_f32_e32 v106, v90
	v_exp_f32_e32 v107, v91
	v_exp_f32_e32 v108, v92
	v_exp_f32_e32 v109, v93
	v_exp_f32_e32 v110, v94
	v_exp_f32_e32 v111, v95
	v_exp_f32_e32 v112, v96
	v_exp_f32_e32 v113, v97
	v_exp_f32_e32 v114, v98
	v_exp_f32_e32 v115, v99
	v_add_f32_e32 v237, v100, v101
	v_add_f32_e32 v251, v102, v103
	v_add_f32_e32 v237, v237, v104
	v_add_f32_e32 v251, v251, v105
	v_add_f32_e32 v237, v237, v106
	v_add_f32_e32 v251, v251, v107
	v_add_f32_e32 v237, v237, v108
	v_add_f32_e32 v251, v251, v109
	v_add_f32_e32 v237, v237, v110
	v_add_f32_e32 v251, v251, v111
	v_add_f32_e32 v237, v237, v112
	v_add_f32_e32 v251, v251, v113
	v_add_f32_e32 v237, v237, v114
	v_add_f32_e32 v251, v251, v115
	v_add_f32_e32 v237, v237, v251
	v_cvt_pk_bf16_f32 v238, v100, v101
	v_cvt_pk_bf16_f32 v239, v102, v103
	v_cvt_pk_bf16_f32 v240, v104, v105
	v_cvt_pk_bf16_f32 v241, v106, v107
	v_cvt_pk_bf16_f32 v242, v108, v109
	v_cvt_pk_bf16_f32 v243, v110, v111
	v_cvt_pk_bf16_f32 v244, v112, v113
	v_cvt_pk_bf16_f32 v245, v114, v115
	s_nop 1
	v_permlane32_swap_b32_e32 v238, v240
	v_permlane32_swap_b32_e32 v239, v241
	v_permlane32_swap_b32_e32 v242, v244
	v_permlane32_swap_b32_e32 v243, v245
	v_exp_f32_e32 v100, v68
	v_exp_f32_e32 v101, v69
	v_exp_f32_e32 v102, v70
	v_exp_f32_e32 v103, v71
	v_exp_f32_e32 v104, v72
	v_exp_f32_e32 v105, v73
	v_exp_f32_e32 v106, v74
	v_exp_f32_e32 v107, v75
	v_exp_f32_e32 v108, v76
	v_exp_f32_e32 v109, v77
	v_exp_f32_e32 v110, v78
	v_exp_f32_e32 v111, v79
	v_exp_f32_e32 v112, v80
	v_exp_f32_e32 v113, v81
	v_exp_f32_e32 v114, v82
	v_exp_f32_e32 v115, v83
	v_add_f32_e32 v250, v100, v101
	v_add_f32_e32 v251, v102, v103
	v_add_f32_e32 v250, v250, v104
	v_add_f32_e32 v251, v251, v105
	v_add_f32_e32 v250, v250, v106
	v_add_f32_e32 v251, v251, v107
	v_add_f32_e32 v250, v250, v108
	v_add_f32_e32 v251, v251, v109
	v_add_f32_e32 v250, v250, v110
	v_add_f32_e32 v251, v251, v111
	v_add_f32_e32 v250, v250, v112
	v_add_f32_e32 v251, v251, v113
	v_add_f32_e32 v250, v250, v114
	v_add_f32_e32 v251, v251, v115
	v_add_f32_e32 v250, v250, v251
	v_cvt_pk_bf16_f32 v100, v100, v101
	v_cvt_pk_bf16_f32 v101, v102, v103
	v_cvt_pk_bf16_f32 v102, v104, v105
	v_cvt_pk_bf16_f32 v103, v106, v107
	v_cvt_pk_bf16_f32 v104, v108, v109
	v_cvt_pk_bf16_f32 v105, v110, v111
	v_cvt_pk_bf16_f32 v106, v112, v113
	v_cvt_pk_bf16_f32 v107, v114, v115
	s_nop 1
	v_permlane32_swap_b32_e32 v100, v102
	v_permlane32_swap_b32_e32 v101, v103
	v_permlane32_swap_b32_e32 v104, v106
	v_permlane32_swap_b32_e32 v105, v107
	s_branch .Lsum_a0b1
.Lsub_a0b1:
	v_sub_f32_e32 v100, v84, v222
	v_sub_f32_e32 v101, v85, v222
	v_sub_f32_e32 v102, v86, v222
	v_sub_f32_e32 v103, v87, v222
	v_sub_f32_e32 v104, v88, v222
	v_sub_f32_e32 v105, v89, v222
	v_sub_f32_e32 v106, v90, v222
	v_sub_f32_e32 v107, v91, v222
	v_sub_f32_e32 v108, v92, v222
	v_sub_f32_e32 v109, v93, v222
	v_sub_f32_e32 v110, v94, v222
	v_sub_f32_e32 v111, v95, v222
	v_sub_f32_e32 v112, v96, v222
	v_sub_f32_e32 v113, v97, v222
	v_sub_f32_e32 v114, v98, v222
	v_sub_f32_e32 v115, v99, v222
	v_exp_f32_e32 v100, v100
	v_exp_f32_e32 v101, v101
	v_exp_f32_e32 v102, v102
	v_exp_f32_e32 v103, v103
	v_exp_f32_e32 v104, v104
	v_exp_f32_e32 v105, v105
	v_exp_f32_e32 v106, v106
	v_exp_f32_e32 v107, v107
	v_exp_f32_e32 v108, v108
	v_exp_f32_e32 v109, v109
	v_exp_f32_e32 v110, v110
	v_exp_f32_e32 v111, v111
	v_exp_f32_e32 v112, v112
	v_exp_f32_e32 v113, v113
	v_exp_f32_e32 v114, v114
	v_exp_f32_e32 v115, v115
	v_add_f32_e32 v237, v100, v101
	v_add_f32_e32 v251, v102, v103
	v_add_f32_e32 v237, v237, v104
	v_add_f32_e32 v251, v251, v105
	v_add_f32_e32 v237, v237, v106
	v_add_f32_e32 v251, v251, v107
	v_add_f32_e32 v237, v237, v108
	v_add_f32_e32 v251, v251, v109
	v_add_f32_e32 v237, v237, v110
	v_add_f32_e32 v251, v251, v111
	v_add_f32_e32 v237, v237, v112
	v_add_f32_e32 v251, v251, v113
	v_add_f32_e32 v237, v237, v114
	v_add_f32_e32 v251, v251, v115
	v_add_f32_e32 v237, v237, v251
	v_cvt_pk_bf16_f32 v238, v100, v101
	v_cvt_pk_bf16_f32 v239, v102, v103
	v_cvt_pk_bf16_f32 v240, v104, v105
	v_cvt_pk_bf16_f32 v241, v106, v107
	v_cvt_pk_bf16_f32 v242, v108, v109
	v_cvt_pk_bf16_f32 v243, v110, v111
	v_cvt_pk_bf16_f32 v244, v112, v113
	v_cvt_pk_bf16_f32 v245, v114, v115
	s_nop 1
	v_permlane32_swap_b32_e32 v238, v240
	v_permlane32_swap_b32_e32 v239, v241
	v_permlane32_swap_b32_e32 v242, v244
	v_permlane32_swap_b32_e32 v243, v245
	v_sub_f32_e32 v100, v68, v222
	v_sub_f32_e32 v101, v69, v222
	v_sub_f32_e32 v102, v70, v222
	v_sub_f32_e32 v103, v71, v222
	v_sub_f32_e32 v104, v72, v222
	v_sub_f32_e32 v105, v73, v222
	v_sub_f32_e32 v106, v74, v222
	v_sub_f32_e32 v107, v75, v222
	v_sub_f32_e32 v108, v76, v222
	v_sub_f32_e32 v109, v77, v222
	v_sub_f32_e32 v110, v78, v222
	v_sub_f32_e32 v111, v79, v222
	v_sub_f32_e32 v112, v80, v222
	v_sub_f32_e32 v113, v81, v222
	v_sub_f32_e32 v114, v82, v222
	v_sub_f32_e32 v115, v83, v222
	v_exp_f32_e32 v100, v100
	v_exp_f32_e32 v101, v101
	v_exp_f32_e32 v102, v102
	v_exp_f32_e32 v103, v103
	v_exp_f32_e32 v104, v104
	v_exp_f32_e32 v105, v105
	v_exp_f32_e32 v106, v106
	v_exp_f32_e32 v107, v107
	v_exp_f32_e32 v108, v108
	v_exp_f32_e32 v109, v109
	v_exp_f32_e32 v110, v110
	v_exp_f32_e32 v111, v111
	v_exp_f32_e32 v112, v112
	v_exp_f32_e32 v113, v113
	v_exp_f32_e32 v114, v114
	v_exp_f32_e32 v115, v115
	v_add_f32_e32 v250, v100, v101
	v_add_f32_e32 v251, v102, v103
	v_add_f32_e32 v250, v250, v104
	v_add_f32_e32 v251, v251, v105
	v_add_f32_e32 v250, v250, v106
	v_add_f32_e32 v251, v251, v107
	v_add_f32_e32 v250, v250, v108
	v_add_f32_e32 v251, v251, v109
	v_add_f32_e32 v250, v250, v110
	v_add_f32_e32 v251, v251, v111
	v_add_f32_e32 v250, v250, v112
	v_add_f32_e32 v251, v251, v113
	v_add_f32_e32 v250, v250, v114
	v_add_f32_e32 v251, v251, v115
	v_add_f32_e32 v250, v250, v251
	v_cvt_pk_bf16_f32 v100, v100, v101
	v_cvt_pk_bf16_f32 v101, v102, v103
	v_cvt_pk_bf16_f32 v102, v104, v105
	v_cvt_pk_bf16_f32 v103, v106, v107
	v_cvt_pk_bf16_f32 v104, v108, v109
	v_cvt_pk_bf16_f32 v105, v110, v111
	v_cvt_pk_bf16_f32 v106, v112, v113
	v_cvt_pk_bf16_f32 v107, v114, v115
	s_nop 1
	v_permlane32_swap_b32_e32 v100, v102
	v_permlane32_swap_b32_e32 v101, v103
	v_permlane32_swap_b32_e32 v104, v106
	v_permlane32_swap_b32_e32 v105, v107
.Lsum_a0b1:
	v_add_f32_e32 v237, v237, v250
	v_cmp_gt_f32_e32 vcc, 0x5f800000, v237
	s_cmp_eq_u64 vcc, exec
	s_cbranch_scc0 .Lfb_a0b1
	v_mov_b32_e32 v250, v237
	s_nop 1
	v_permlane32_swap_b32_e32 v237, v250
	v_add_f32_e32 v237, v237, v250
	v_add_f32_e32 v221, v237, v221
	v_mov_b32_e32 v223, v222
	s_waitcnt lgkmcnt(6)
	v_mfma_f32_32x32x16_bf16 v[52:67], v[116:119], v[238:241], v[52:67]
	ds_read_b64_tr_b16 v[116:117], v191 offset:16896
	ds_read_b64_tr_b16 v[118:119], v191 offset:18944
	s_waitcnt lgkmcnt(6)
	v_mfma_f32_32x32x16_bf16 v[52:67], v[120:123], v[242:245], v[52:67]
	ds_read_b64_tr_b16 v[120:121], v191 offset:20992
	ds_read_b64_tr_b16 v[122:123], v191 offset:23040
	s_waitcnt lgkmcnt(6)
	v_mfma_f32_32x32x16_bf16 v[52:67], v[124:127], v[100:103], v[52:67]
	ds_read_b64_tr_b16 v[124:125], v191 offset:25088
	ds_read_b64_tr_b16 v[126:127], v191 offset:27136
	s_waitcnt lgkmcnt(6)
	v_mfma_f32_32x32x16_bf16 v[52:67], v[128:131], v[104:107], v[52:67]
	ds_read_b64_tr_b16 v[128:129], v191 offset:29184
	ds_read_b64_tr_b16 v[130:131], v191 offset:31232
	s_waitcnt lgkmcnt(6)
	v_mfma_f32_32x32x16_bf16 v[36:51], v[116:119], v[238:241], v[36:51]
	ds_read_b64_tr_b16 v[116:117], v191 offset:17408
	ds_read_b64_tr_b16 v[118:119], v191 offset:19456
	s_waitcnt lgkmcnt(6)
	v_mfma_f32_32x32x16_bf16 v[36:51], v[120:123], v[242:245], v[36:51]
	ds_read_b64_tr_b16 v[120:121], v191 offset:21504
	ds_read_b64_tr_b16 v[122:123], v191 offset:23552
	s_waitcnt lgkmcnt(6)
	v_mfma_f32_32x32x16_bf16 v[36:51], v[124:127], v[100:103], v[36:51]
	ds_read_b64_tr_b16 v[124:125], v191 offset:25600
	ds_read_b64_tr_b16 v[126:127], v191 offset:27648
	s_waitcnt lgkmcnt(6)
	v_mfma_f32_32x32x16_bf16 v[36:51], v[128:131], v[104:107], v[36:51]
	ds_read_b64_tr_b16 v[128:129], v191 offset:29696
	ds_read_b64_tr_b16 v[130:131], v191 offset:31744
	s_waitcnt lgkmcnt(6)
	v_mfma_f32_32x32x16_bf16 v[20:35], v[116:119], v[238:241], v[20:35]
	ds_read_b64_tr_b16 v[116:117], v191 offset:17920
	ds_read_b64_tr_b16 v[118:119], v191 offset:19968
	s_waitcnt lgkmcnt(6)
	v_mfma_f32_32x32x16_bf16 v[20:35], v[120:123], v[242:245], v[20:35]
	ds_read_b64_tr_b16 v[120:121], v191 offset:22016
	ds_read_b64_tr_b16 v[122:123], v191 offset:24064
	s_waitcnt lgkmcnt(6)
	v_mfma_f32_32x32x16_bf16 v[20:35], v[124:127], v[100:103], v[20:35]
	ds_read_b64_tr_b16 v[124:125], v191 offset:26112
	ds_read_b64_tr_b16 v[126:127], v191 offset:28160
	s_waitcnt lgkmcnt(6)
	v_mfma_f32_32x32x16_bf16 v[20:35], v[128:131], v[104:107], v[20:35]
	ds_read_b64_tr_b16 v[128:129], v191 offset:30208
	ds_read_b64_tr_b16 v[130:131], v191 offset:32256
	s_waitcnt lgkmcnt(6)
	v_mfma_f32_32x32x16_bf16 v[4:19], v[116:119], v[238:241], v[4:19]
	s_waitcnt lgkmcnt(4)
	v_mfma_f32_32x32x16_bf16 v[4:19], v[120:123], v[242:245], v[4:19]
	s_waitcnt lgkmcnt(2)
	v_mfma_f32_32x32x16_bf16 v[4:19], v[124:127], v[100:103], v[4:19]
	s_waitcnt lgkmcnt(0)
	v_mfma_f32_32x32x16_bf16 v[4:19], v[128:131], v[104:107], v[4:19]
	s_setprio 0
	s_branch .Ltail2_a0b1

.LBB0_579:
	v_add_f32_e32 v100, v84, v85
	ds_read_b64_tr_b16 v[84:85], v191 offset:0x4000
	ds_read_b64_tr_b16 v[86:87], v191 offset:0x4800
	ds_read_b64_tr_b16 v[88:89], v191 offset:0x5000
	ds_read_b64_tr_b16 v[90:91], v191 offset:0x5800
	ds_read_b64_tr_b16 v[92:93], v191 offset:0x6000
	ds_read_b64_tr_b16 v[94:95], v191 offset:0x6800
	ds_read_b64_tr_b16 v[96:97], v191 offset:0x7000
	ds_read_b64_tr_b16 v[98:99], v191 offset:0x7800
	v_fmac_f32_e32 v100, v221, v2
	s_waitcnt lgkmcnt(6)
	v_mfma_f32_32x32x16_bf16 v[52:67], v[84:87], v[68:71], v[52:67]
	ds_read_b64_tr_b16 v[84:85], v191 offset:0x4200
	ds_read_b64_tr_b16 v[86:87], v191 offset:0x4a00
	s_waitcnt lgkmcnt(6)
	v_mfma_f32_32x32x16_bf16 v[52:67], v[88:91], v[72:75], v[52:67]
	ds_read_b64_tr_b16 v[88:89], v191 offset:0x5200
	ds_read_b64_tr_b16 v[90:91], v191 offset:0x5a00
	s_waitcnt lgkmcnt(6)
	v_mfma_f32_32x32x16_bf16 v[52:67], v[92:95], v[76:79], v[52:67]
	ds_read_b64_tr_b16 v[92:93], v191 offset:0x6200
	ds_read_b64_tr_b16 v[94:95], v191 offset:0x6a00
	s_waitcnt lgkmcnt(6)
	v_mfma_f32_32x32x16_bf16 v[52:67], v[96:99], v[80:83], v[52:67]
	ds_read_b64_tr_b16 v[96:97], v191 offset:0x7200
	ds_read_b64_tr_b16 v[98:99], v191 offset:0x7a00
	s_waitcnt lgkmcnt(6)
	v_mfma_f32_32x32x16_bf16 v[36:51], v[84:87], v[68:71], v[36:51]
	ds_read_b64_tr_b16 v[84:85], v191 offset:0x4400
	ds_read_b64_tr_b16 v[86:87], v191 offset:0x4c00
	s_waitcnt lgkmcnt(6)
	v_mfma_f32_32x32x16_bf16 v[36:51], v[88:91], v[72:75], v[36:51]
	ds_read_b64_tr_b16 v[88:89], v191 offset:0x5400
	ds_read_b64_tr_b16 v[90:91], v191 offset:0x5c00
	s_waitcnt lgkmcnt(6)
	v_mfma_f32_32x32x16_bf16 v[36:51], v[92:95], v[76:79], v[36:51]
	ds_read_b64_tr_b16 v[92:93], v191 offset:0x6400
	ds_read_b64_tr_b16 v[94:95], v191 offset:0x6c00
	s_waitcnt lgkmcnt(6)
	v_mfma_f32_32x32x16_bf16 v[36:51], v[96:99], v[80:83], v[36:51]
	ds_read_b64_tr_b16 v[96:97], v191 offset:0x7400
	ds_read_b64_tr_b16 v[98:99], v191 offset:0x7c00
	s_waitcnt lgkmcnt(6)
	v_mfma_f32_32x32x16_bf16 v[20:35], v[84:87], v[68:71], v[20:35]
	ds_read_b64_tr_b16 v[84:85], v191 offset:0x4600
	ds_read_b64_tr_b16 v[86:87], v191 offset:0x4e00
	s_waitcnt lgkmcnt(6)
	v_mfma_f32_32x32x16_bf16 v[20:35], v[88:91], v[72:75], v[20:35]
	ds_read_b64_tr_b16 v[88:89], v191 offset:0x5600
	ds_read_b64_tr_b16 v[90:91], v191 offset:0x5e00
	s_waitcnt lgkmcnt(6)
	v_mfma_f32_32x32x16_bf16 v[20:35], v[92:95], v[76:79], v[20:35]
	ds_read_b64_tr_b16 v[92:93], v191 offset:0x6600
	ds_read_b64_tr_b16 v[94:95], v191 offset:0x6e00
	s_waitcnt lgkmcnt(6)
	v_mfma_f32_32x32x16_bf16 v[20:35], v[96:99], v[80:83], v[20:35]
	ds_read_b64_tr_b16 v[96:97], v191 offset:0x7600
	ds_read_b64_tr_b16 v[98:99], v191 offset:0x7e00
	s_waitcnt lgkmcnt(6)
	v_mfma_f32_32x32x16_bf16 v[4:19], v[84:87], v[68:71], v[4:19]
	s_waitcnt lgkmcnt(4)
	v_mfma_f32_32x32x16_bf16 v[4:19], v[88:91], v[72:75], v[4:19]
	s_waitcnt lgkmcnt(2)
	v_mfma_f32_32x32x16_bf16 v[4:19], v[92:95], v[76:79], v[4:19]
	s_waitcnt lgkmcnt(0)
	v_mfma_f32_32x32x16_bf16 v[4:19], v[96:99], v[80:83], v[4:19]
	s_setprio 0
	v_mov_b32_e32 v221, v100
.Ltail2_a0b1:
	s_branch .LBB0_533

.LBB0_1452:
	s_cmp_le_i32 s18, s40
	s_cbranch_scc0 .Lorig_a1b0
	s_cmp_eq_u32 s71, 0
	s_cbranch_scc1 .Lorig_a1b0
	ds_read_b128 v[140:143], v176
	ds_read_b128 v[144:147], v176 offset:32
	ds_read_b128 v[148:151], v176 offset:64
	ds_read_b128 v[152:155], v176 offset:96
	ds_read_b128 v[208:211], v172 offset:32768
	ds_read_b128 v[212:215], v206 offset:32768
	ds_read_b128 v[216:219], v207 offset:32768
	ds_read_b128 v[220:223], v237 offset:32768
	ds_read_b128 v[156:159], v176 offset:128
	ds_read_b128 v[160:163], v176 offset:160
	ds_read_b128 v[164:167], v176 offset:192
	ds_read_b128 v[168:171], v176 offset:224
	s_waitcnt lgkmcnt(7)
	v_mfma_f32_32x32x16_bf16 v[84:99], v[208:211], v[100:103], v[140:155]
	ds_read_b128 v[208:211], v244 offset:32768
	s_waitcnt lgkmcnt(7)
	v_mfma_f32_32x32x16_bf16 v[84:99], v[212:215], v[104:107], v[84:99]
	ds_read_b128 v[212:215], v245 offset:32768
	s_waitcnt lgkmcnt(7)
	v_mfma_f32_32x32x16_bf16 v[84:99], v[216:219], v[108:111], v[84:99]
	ds_read_b128 v[216:219], v246 offset:32768
	s_waitcnt lgkmcnt(7)
	v_mfma_f32_32x32x16_bf16 v[84:99], v[220:223], v[112:115], v[84:99]
	ds_read_b128 v[220:223], v247 offset:32768
	s_waitcnt lgkmcnt(3)
	v_mfma_f32_32x32x16_bf16 v[84:99], v[208:211], v[116:119], v[84:99]
	ds_read_b128 v[208:211], v172 offset:40960
	s_waitcnt lgkmcnt(3)
	v_mfma_f32_32x32x16_bf16 v[84:99], v[212:215], v[120:123], v[84:99]
	ds_read_b128 v[212:215], v206 offset:40960
	s_waitcnt lgkmcnt(3)
	v_mfma_f32_32x32x16_bf16 v[84:99], v[216:219], v[124:127], v[84:99]
	ds_read_b128 v[216:219], v207 offset:40960
	s_waitcnt lgkmcnt(3)
	v_mfma_f32_32x32x16_bf16 v[84:99], v[220:223], v[128:131], v[84:99]
	ds_read_b128 v[220:223], v237 offset:40960
	s_waitcnt lgkmcnt(3)
	v_mfma_f32_32x32x16_bf16 v[68:83], v[208:211], v[100:103], v[156:171]
	ds_read_b128 v[208:211], v244 offset:40960
	s_waitcnt lgkmcnt(3)
	v_mfma_f32_32x32x16_bf16 v[68:83], v[212:215], v[104:107], v[68:83]
	ds_read_b128 v[212:215], v245 offset:40960
	s_waitcnt lgkmcnt(3)
	v_mfma_f32_32x32x16_bf16 v[68:83], v[216:219], v[108:111], v[68:83]
	ds_read_b128 v[216:219], v246 offset:40960
	s_waitcnt lgkmcnt(3)
	v_mfma_f32_32x32x16_bf16 v[68:83], v[220:223], v[112:115], v[68:83]
	ds_read_b128 v[220:223], v247 offset:40960
	s_waitcnt lgkmcnt(3)
	v_mfma_f32_32x32x16_bf16 v[68:83], v[208:211], v[116:119], v[68:83]
	s_waitcnt lgkmcnt(2)
	v_mfma_f32_32x32x16_bf16 v[68:83], v[212:215], v[120:123], v[68:83]
	s_waitcnt lgkmcnt(1)
	v_mfma_f32_32x32x16_bf16 v[68:83], v[216:219], v[124:127], v[68:83]
	s_waitcnt lgkmcnt(0)
	v_mfma_f32_32x32x16_bf16 v[68:83], v[220:223], v[128:131], v[68:83]
	ds_read_b64_tr_b16 v[208:209], v174 offset:0
	ds_read_b64_tr_b16 v[210:211], v174 offset:2048
	ds_read_b64_tr_b16 v[212:213], v174 offset:4096
	ds_read_b64_tr_b16 v[214:215], v174 offset:6144
	ds_read_b64_tr_b16 v[216:217], v174 offset:8192
	ds_read_b64_tr_b16 v[218:219], v174 offset:10240
	ds_read_b64_tr_b16 v[220:221], v174 offset:12288
	ds_read_b64_tr_b16 v[222:223], v174 offset:14336
	s_nop 7
	s_nop 3
	v_cmp_eq_f32_e32 vcc, 0, v193
	s_cmp_eq_u64 vcc, exec
	s_cbranch_scc0 .Lsub_a1b0
	v_exp_f32_e32 v140, v84
	v_exp_f32_e32 v141, v85
	v_exp_f32_e32 v142, v86
	v_exp_f32_e32 v143, v87
	v_exp_f32_e32 v144, v88
	v_exp_f32_e32 v145, v89
	v_exp_f32_e32 v146, v90
	v_exp_f32_e32 v147, v91
	v_exp_f32_e32 v148, v92
	v_exp_f32_e32 v149, v93
	v_exp_f32_e32 v150, v94
	v_exp_f32_e32 v151, v95
	v_exp_f32_e32 v152, v96
	v_exp_f32_e32 v153, v97
	v_exp_f32_e32 v154, v98
	v_exp_f32_e32 v155, v99
	v_add_f32_e32 v248, v140, v141
	v_add_f32_e32 v250, v142, v143
	v_add_f32_e32 v248, v248, v144
	v_add_f32_e32 v250, v250, v145
	v_add_f32_e32 v248, v248, v146
	v_add_f32_e32 v250, v250, v147
	v_add_f32_e32 v248, v248, v148
	v_add_f32_e32 v250, v250, v149
	v_add_f32_e32 v248, v248, v150
	v_add_f32_e32 v250, v250, v151
	v_add_f32_e32 v248, v248, v152
	v_add_f32_e32 v250, v250, v153
	v_add_f32_e32 v248, v248, v154
	v_add_f32_e32 v250, v250, v155
	v_add_f32_e32 v248, v248, v250
	v_cvt_pk_bf16_f32 v140, v140, v141
	v_cvt_pk_bf16_f32 v141, v142, v143
	v_cvt_pk_bf16_f32 v142, v144, v145
	v_cvt_pk_bf16_f32 v143, v146, v147
	v_cvt_pk_bf16_f32 v144, v148, v149
	v_cvt_pk_bf16_f32 v145, v150, v151
	v_cvt_pk_bf16_f32 v146, v152, v153
	v_cvt_pk_bf16_f32 v147, v154, v155
	s_nop 1
	v_permlane32_swap_b32_e32 v140, v142
	v_permlane32_swap_b32_e32 v141, v143
	v_permlane32_swap_b32_e32 v144, v146
	v_permlane32_swap_b32_e32 v145, v147
	v_exp_f32_e32 v156, v68
	v_exp_f32_e32 v157, v69
	v_exp_f32_e32 v158, v70
	v_exp_f32_e32 v159, v71
	v_exp_f32_e32 v160, v72
	v_exp_f32_e32 v161, v73
	v_exp_f32_e32 v162, v74
	v_exp_f32_e32 v163, v75
	v_exp_f32_e32 v164, v76
	v_exp_f32_e32 v165, v77
	v_exp_f32_e32 v166, v78
	v_exp_f32_e32 v167, v79
	v_exp_f32_e32 v168, v80
	v_exp_f32_e32 v169, v81
	v_exp_f32_e32 v170, v82
	v_exp_f32_e32 v171, v83
	v_add_f32_e32 v249, v156, v157
	v_add_f32_e32 v250, v158, v159
	v_add_f32_e32 v249, v249, v160
	v_add_f32_e32 v250, v250, v161
	v_add_f32_e32 v249, v249, v162
	v_add_f32_e32 v250, v250, v163
	v_add_f32_e32 v249, v249, v164
	v_add_f32_e32 v250, v250, v165
	v_add_f32_e32 v249, v249, v166
	v_add_f32_e32 v250, v250, v167
	v_add_f32_e32 v249, v249, v168
	v_add_f32_e32 v250, v250, v169
	v_add_f32_e32 v249, v249, v170
	v_add_f32_e32 v250, v250, v171
	v_add_f32_e32 v249, v249, v250
	v_cvt_pk_bf16_f32 v156, v156, v157
	v_cvt_pk_bf16_f32 v157, v158, v159
	v_cvt_pk_bf16_f32 v158, v160, v161
	v_cvt_pk_bf16_f32 v159, v162, v163
	v_cvt_pk_bf16_f32 v160, v164, v165
	v_cvt_pk_bf16_f32 v161, v166, v167
	v_cvt_pk_bf16_f32 v162, v168, v169
	v_cvt_pk_bf16_f32 v163, v170, v171
	s_nop 1
	v_permlane32_swap_b32_e32 v156, v158
	v_permlane32_swap_b32_e32 v157, v159
	v_permlane32_swap_b32_e32 v160, v162
	v_permlane32_swap_b32_e32 v161, v163
	s_branch .Lsum_a1b0
.Lsub_a1b0:
	v_sub_f32_e32 v140, v84, v193
	v_sub_f32_e32 v141, v85, v193
	v_sub_f32_e32 v142, v86, v193
	v_sub_f32_e32 v143, v87, v193
	v_sub_f32_e32 v144, v88, v193
	v_sub_f32_e32 v145, v89, v193
	v_sub_f32_e32 v146, v90, v193
	v_sub_f32_e32 v147, v91, v193
	v_sub_f32_e32 v148, v92, v193
	v_sub_f32_e32 v149, v93, v193
	v_sub_f32_e32 v150, v94, v193
	v_sub_f32_e32 v151, v95, v193
	v_sub_f32_e32 v152, v96, v193
	v_sub_f32_e32 v153, v97, v193
	v_sub_f32_e32 v154, v98, v193
	v_sub_f32_e32 v155, v99, v193
	v_exp_f32_e32 v140, v140
	v_exp_f32_e32 v141, v141
	v_exp_f32_e32 v142, v142
	v_exp_f32_e32 v143, v143
	v_exp_f32_e32 v144, v144
	v_exp_f32_e32 v145, v145
	v_exp_f32_e32 v146, v146
	v_exp_f32_e32 v147, v147
	v_exp_f32_e32 v148, v148
	v_exp_f32_e32 v149, v149
	v_exp_f32_e32 v150, v150
	v_exp_f32_e32 v151, v151
	v_exp_f32_e32 v152, v152
	v_exp_f32_e32 v153, v153
	v_exp_f32_e32 v154, v154
	v_exp_f32_e32 v155, v155
	v_add_f32_e32 v248, v140, v141
	v_add_f32_e32 v250, v142, v143
	v_add_f32_e32 v248, v248, v144
	v_add_f32_e32 v250, v250, v145
	v_add_f32_e32 v248, v248, v146
	v_add_f32_e32 v250, v250, v147
	v_add_f32_e32 v248, v248, v148
	v_add_f32_e32 v250, v250, v149
	v_add_f32_e32 v248, v248, v150
	v_add_f32_e32 v250, v250, v151
	v_add_f32_e32 v248, v248, v152
	v_add_f32_e32 v250, v250, v153
	v_add_f32_e32 v248, v248, v154
	v_add_f32_e32 v250, v250, v155
	v_add_f32_e32 v248, v248, v250
	v_cvt_pk_bf16_f32 v140, v140, v141
	v_cvt_pk_bf16_f32 v141, v142, v143
	v_cvt_pk_bf16_f32 v142, v144, v145
	v_cvt_pk_bf16_f32 v143, v146, v147
	v_cvt_pk_bf16_f32 v144, v148, v149
	v_cvt_pk_bf16_f32 v145, v150, v151
	v_cvt_pk_bf16_f32 v146, v152, v153
	v_cvt_pk_bf16_f32 v147, v154, v155
	s_nop 1
	v_permlane32_swap_b32_e32 v140, v142
	v_permlane32_swap_b32_e32 v141, v143
	v_permlane32_swap_b32_e32 v144, v146
	v_permlane32_swap_b32_e32 v145, v147
	v_sub_f32_e32 v156, v68, v193
	v_sub_f32_e32 v157, v69, v193
	v_sub_f32_e32 v158, v70, v193
	v_sub_f32_e32 v159, v71, v193
	v_sub_f32_e32 v160, v72, v193
	v_sub_f32_e32 v161, v73, v193
	v_sub_f32_e32 v162, v74, v193
	v_sub_f32_e32 v163, v75, v193
	v_sub_f32_e32 v164, v76, v193
	v_sub_f32_e32 v165, v77, v193
	v_sub_f32_e32 v166, v78, v193
	v_sub_f32_e32 v167, v79, v193
	v_sub_f32_e32 v168, v80, v193
	v_sub_f32_e32 v169, v81, v193
	v_sub_f32_e32 v170, v82, v193
	v_sub_f32_e32 v171, v83, v193
	v_exp_f32_e32 v156, v156
	v_exp_f32_e32 v157, v157
	v_exp_f32_e32 v158, v158
	v_exp_f32_e32 v159, v159
	v_exp_f32_e32 v160, v160
	v_exp_f32_e32 v161, v161
	v_exp_f32_e32 v162, v162
	v_exp_f32_e32 v163, v163
	v_exp_f32_e32 v164, v164
	v_exp_f32_e32 v165, v165
	v_exp_f32_e32 v166, v166
	v_exp_f32_e32 v167, v167
	v_exp_f32_e32 v168, v168
	v_exp_f32_e32 v169, v169
	v_exp_f32_e32 v170, v170
	v_exp_f32_e32 v171, v171
	v_add_f32_e32 v249, v156, v157
	v_add_f32_e32 v250, v158, v159
	v_add_f32_e32 v249, v249, v160
	v_add_f32_e32 v250, v250, v161
	v_add_f32_e32 v249, v249, v162
	v_add_f32_e32 v250, v250, v163
	v_add_f32_e32 v249, v249, v164
	v_add_f32_e32 v250, v250, v165
	v_add_f32_e32 v249, v249, v166
	v_add_f32_e32 v250, v250, v167
	v_add_f32_e32 v249, v249, v168
	v_add_f32_e32 v250, v250, v169
	v_add_f32_e32 v249, v249, v170
	v_add_f32_e32 v250, v250, v171
	v_add_f32_e32 v249, v249, v250
	v_cvt_pk_bf16_f32 v156, v156, v157
	v_cvt_pk_bf16_f32 v157, v158, v159
	v_cvt_pk_bf16_f32 v158, v160, v161
	v_cvt_pk_bf16_f32 v159, v162, v163
	v_cvt_pk_bf16_f32 v160, v164, v165
	v_cvt_pk_bf16_f32 v161, v166, v167
	v_cvt_pk_bf16_f32 v162, v168, v169
	v_cvt_pk_bf16_f32 v163, v170, v171
	s_nop 1
	v_permlane32_swap_b32_e32 v156, v158
	v_permlane32_swap_b32_e32 v157, v159
	v_permlane32_swap_b32_e32 v160, v162
	v_permlane32_swap_b32_e32 v161, v163
.Lsum_a1b0:
	v_add_f32_e32 v248, v248, v249
	v_cmp_gt_f32_e32 vcc, 0x5f800000, v248
	s_cmp_eq_u64 vcc, exec
	s_cbranch_scc0 .Lfb_a1b0
	v_mov_b32_e32 v249, v248
	s_nop 1
	v_permlane32_swap_b32_e32 v248, v249
	v_add_f32_e32 v248, v248, v249
	v_add_f32_e32 v191, v248, v191
	v_mov_b32_e32 v192, v193
	s_waitcnt lgkmcnt(6)
	v_mfma_f32_32x32x16_bf16 v[52:67], v[208:211], v[140:143], v[52:67]
	ds_read_b64_tr_b16 v[208:209], v174 offset:512
	ds_read_b64_tr_b16 v[210:211], v174 offset:2560
	s_waitcnt lgkmcnt(6)
	v_mfma_f32_32x32x16_bf16 v[52:67], v[212:215], v[144:147], v[52:67]
	ds_read_b64_tr_b16 v[212:213], v174 offset:4608
	ds_read_b64_tr_b16 v[214:215], v174 offset:6656
	s_waitcnt lgkmcnt(6)
	v_mfma_f32_32x32x16_bf16 v[52:67], v[216:219], v[156:159], v[52:67]
	ds_read_b64_tr_b16 v[216:217], v174 offset:8704
	ds_read_b64_tr_b16 v[218:219], v174 offset:10752
	s_waitcnt lgkmcnt(6)
	v_mfma_f32_32x32x16_bf16 v[52:67], v[220:223], v[160:163], v[52:67]
	ds_read_b64_tr_b16 v[220:221], v174 offset:12800
	ds_read_b64_tr_b16 v[222:223], v174 offset:14848
	s_waitcnt lgkmcnt(6)
	v_mfma_f32_32x32x16_bf16 v[36:51], v[208:211], v[140:143], v[36:51]
	ds_read_b64_tr_b16 v[208:209], v174 offset:1024
	ds_read_b64_tr_b16 v[210:211], v174 offset:3072
	s_waitcnt lgkmcnt(6)
	v_mfma_f32_32x32x16_bf16 v[36:51], v[212:215], v[144:147], v[36:51]
	ds_read_b64_tr_b16 v[212:213], v174 offset:5120
	ds_read_b64_tr_b16 v[214:215], v174 offset:7168
	s_waitcnt lgkmcnt(6)
	v_mfma_f32_32x32x16_bf16 v[36:51], v[216:219], v[156:159], v[36:51]
	ds_read_b64_tr_b16 v[216:217], v174 offset:9216
	ds_read_b64_tr_b16 v[218:219], v174 offset:11264
	s_waitcnt lgkmcnt(6)
	v_mfma_f32_32x32x16_bf16 v[36:51], v[220:223], v[160:163], v[36:51]
	ds_read_b64_tr_b16 v[220:221], v174 offset:13312
	ds_read_b64_tr_b16 v[222:223], v174 offset:15360
	s_waitcnt lgkmcnt(6)
	v_mfma_f32_32x32x16_bf16 v[20:35], v[208:211], v[140:143], v[20:35]
	ds_read_b64_tr_b16 v[208:209], v174 offset:1536
	ds_read_b64_tr_b16 v[210:211], v174 offset:3584
	s_waitcnt lgkmcnt(6)
	v_mfma_f32_32x32x16_bf16 v[20:35], v[212:215], v[144:147], v[20:35]
	ds_read_b64_tr_b16 v[212:213], v174 offset:5632
	ds_read_b64_tr_b16 v[214:215], v174 offset:7680
	s_waitcnt lgkmcnt(6)
	v_mfma_f32_32x32x16_bf16 v[20:35], v[216:219], v[156:159], v[20:35]
	ds_read_b64_tr_b16 v[216:217], v174 offset:9728
	ds_read_b64_tr_b16 v[218:219], v174 offset:11776
	s_waitcnt lgkmcnt(6)
	v_mfma_f32_32x32x16_bf16 v[20:35], v[220:223], v[160:163], v[20:35]
	ds_read_b64_tr_b16 v[220:221], v174 offset:13824
	ds_read_b64_tr_b16 v[222:223], v174 offset:15872
	s_waitcnt lgkmcnt(6)
	v_mfma_f32_32x32x16_bf16 v[4:19], v[208:211], v[140:143], v[4:19]
	s_waitcnt lgkmcnt(4)
	v_mfma_f32_32x32x16_bf16 v[4:19], v[212:215], v[144:147], v[4:19]
	s_waitcnt lgkmcnt(2)
	v_mfma_f32_32x32x16_bf16 v[4:19], v[216:219], v[156:159], v[4:19]
	s_waitcnt lgkmcnt(0)
	v_mfma_f32_32x32x16_bf16 v[4:19], v[220:223], v[160:163], v[4:19]
	s_setprio 0
	s_branch .Ltail2_a1b0
.Lfb_a1b0:
	s_waitcnt lgkmcnt(0)
	v_mov_b64_e32 v[166:167], v[84:85]
	v_mov_b64_e32 v[160:161], v[86:87]
	v_mov_b64_e32 v[154:155], v[88:89]
	v_mov_b64_e32 v[150:151], v[90:91]
	v_mov_b64_e32 v[144:145], v[92:93]
	v_mov_b64_e32 v[146:147], v[94:95]
	v_mov_b64_e32 v[142:143], v[96:97]
	v_mov_b64_e32 v[140:141], v[98:99]
	v_mov_b64_e32 v[170:171], v[68:69]
	v_mov_b64_e32 v[168:169], v[70:71]
	v_mov_b64_e32 v[164:165], v[72:73]
	v_mov_b64_e32 v[162:163], v[74:75]
	v_mov_b64_e32 v[156:157], v[76:77]
	v_mov_b64_e32 v[158:159], v[78:79]
	v_mov_b64_e32 v[152:153], v[80:81]
	v_mov_b64_e32 v[148:149], v[82:83]
	s_branch .LBB0_1454

.LBB0_1467:
	s_add_i32 s98, s18, 64
	s_cmp_le_i32 s98, s40
	s_cbranch_scc0 .Lorig_a1b1
	ds_read_b128 v[140:143], v177
	ds_read_b128 v[144:147], v177 offset:32
	ds_read_b128 v[148:151], v177 offset:64
	ds_read_b128 v[152:155], v177 offset:96
	ds_read_b128 v[208:211], v172 offset:49152
	ds_read_b128 v[212:215], v206 offset:49152
	ds_read_b128 v[216:219], v207 offset:49152
	ds_read_b128 v[220:223], v237 offset:49152
	ds_read_b128 v[156:159], v177 offset:128
	ds_read_b128 v[160:163], v177 offset:160
	ds_read_b128 v[164:167], v177 offset:192
	ds_read_b128 v[168:171], v177 offset:224
	s_waitcnt lgkmcnt(7)
	v_mfma_f32_32x32x16_bf16 v[84:99], v[208:211], v[100:103], v[140:155]
	ds_read_b128 v[208:211], v244 offset:49152
	s_waitcnt lgkmcnt(7)
	v_mfma_f32_32x32x16_bf16 v[84:99], v[212:215], v[104:107], v[84:99]
	ds_read_b128 v[212:215], v245 offset:49152
	s_waitcnt lgkmcnt(7)
	v_mfma_f32_32x32x16_bf16 v[84:99], v[216:219], v[108:111], v[84:99]
	ds_read_b128 v[216:219], v246 offset:49152
	s_waitcnt lgkmcnt(7)
	v_mfma_f32_32x32x16_bf16 v[84:99], v[220:223], v[112:115], v[84:99]
	ds_read_b128 v[220:223], v247 offset:49152
	s_waitcnt lgkmcnt(3)
	v_mfma_f32_32x32x16_bf16 v[84:99], v[208:211], v[116:119], v[84:99]
	ds_read_b128 v[208:211], v172 offset:57344
	s_waitcnt lgkmcnt(3)
	v_mfma_f32_32x32x16_bf16 v[84:99], v[212:215], v[120:123], v[84:99]
	ds_read_b128 v[212:215], v206 offset:57344
	s_waitcnt lgkmcnt(3)
	v_mfma_f32_32x32x16_bf16 v[84:99], v[216:219], v[124:127], v[84:99]
	ds_read_b128 v[216:219], v207 offset:57344
	s_waitcnt lgkmcnt(3)
	v_mfma_f32_32x32x16_bf16 v[84:99], v[220:223], v[128:131], v[84:99]
	ds_read_b128 v[220:223], v237 offset:57344
	s_waitcnt lgkmcnt(3)
	v_mfma_f32_32x32x16_bf16 v[68:83], v[208:211], v[100:103], v[156:171]
	ds_read_b128 v[208:211], v244 offset:57344
	s_waitcnt lgkmcnt(3)
	v_mfma_f32_32x32x16_bf16 v[68:83], v[212:215], v[104:107], v[68:83]
	ds_read_b128 v[212:215], v245 offset:57344
	s_waitcnt lgkmcnt(3)
	v_mfma_f32_32x32x16_bf16 v[68:83], v[216:219], v[108:111], v[68:83]
	ds_read_b128 v[216:219], v246 offset:57344
	s_waitcnt lgkmcnt(3)
	v_mfma_f32_32x32x16_bf16 v[68:83], v[220:223], v[112:115], v[68:83]
	ds_read_b128 v[220:223], v247 offset:57344
	s_waitcnt lgkmcnt(3)
	v_mfma_f32_32x32x16_bf16 v[68:83], v[208:211], v[116:119], v[68:83]
	s_waitcnt lgkmcnt(2)
	v_mfma_f32_32x32x16_bf16 v[68:83], v[212:215], v[120:123], v[68:83]
	s_waitcnt lgkmcnt(1)
	v_mfma_f32_32x32x16_bf16 v[68:83], v[216:219], v[124:127], v[68:83]
	s_waitcnt lgkmcnt(0)
	v_mfma_f32_32x32x16_bf16 v[68:83], v[220:223], v[128:131], v[68:83]
	ds_read_b64_tr_b16 v[208:209], v174 offset:16384
	ds_read_b64_tr_b16 v[210:211], v174 offset:18432
	ds_read_b64_tr_b16 v[212:213], v174 offset:20480
	ds_read_b64_tr_b16 v[214:215], v174 offset:22528
	ds_read_b64_tr_b16 v[216:217], v174 offset:24576
	ds_read_b64_tr_b16 v[218:219], v174 offset:26624
	ds_read_b64_tr_b16 v[220:221], v174 offset:28672
	ds_read_b64_tr_b16 v[222:223], v174 offset:30720
	s_nop 7
	s_nop 3
	v_cmp_eq_f32_e32 vcc, 0, v192
	s_cmp_eq_u64 vcc, exec
	s_cbranch_scc0 .Lsub_a1b1
	v_exp_f32_e32 v140, v84
	v_exp_f32_e32 v141, v85
	v_exp_f32_e32 v142, v86
	v_exp_f32_e32 v143, v87
	v_exp_f32_e32 v144, v88
	v_exp_f32_e32 v145, v89
	v_exp_f32_e32 v146, v90
	v_exp_f32_e32 v147, v91
	v_exp_f32_e32 v148, v92
	v_exp_f32_e32 v149, v93
	v_exp_f32_e32 v150, v94
	v_exp_f32_e32 v151, v95
	v_exp_f32_e32 v152, v96
	v_exp_f32_e32 v153, v97
	v_exp_f32_e32 v154, v98
	v_exp_f32_e32 v155, v99
	v_add_f32_e32 v248, v140, v141
	v_add_f32_e32 v250, v142, v143
	v_add_f32_e32 v248, v248, v144
	v_add_f32_e32 v250, v250, v145
	v_add_f32_e32 v248, v248, v146
	v_add_f32_e32 v250, v250, v147
	v_add_f32_e32 v248, v248, v148
	v_add_f32_e32 v250, v250, v149
	v_add_f32_e32 v248, v248, v150
	v_add_f32_e32 v250, v250, v151
	v_add_f32_e32 v248, v248, v152
	v_add_f32_e32 v250, v250, v153
	v_add_f32_e32 v248, v248, v154
	v_add_f32_e32 v250, v250, v155
	v_add_f32_e32 v248, v248, v250
	v_cvt_pk_bf16_f32 v140, v140, v141
	v_cvt_pk_bf16_f32 v141, v142, v143
	v_cvt_pk_bf16_f32 v142, v144, v145
	v_cvt_pk_bf16_f32 v143, v146, v147
	v_cvt_pk_bf16_f32 v144, v148, v149
	v_cvt_pk_bf16_f32 v145, v150, v151
	v_cvt_pk_bf16_f32 v146, v152, v153
	v_cvt_pk_bf16_f32 v147, v154, v155
	s_nop 1
	v_permlane32_swap_b32_e32 v140, v142
	v_permlane32_swap_b32_e32 v141, v143
	v_permlane32_swap_b32_e32 v144, v146
	v_permlane32_swap_b32_e32 v145, v147
	v_exp_f32_e32 v156, v68
	v_exp_f32_e32 v157, v69
	v_exp_f32_e32 v158, v70
	v_exp_f32_e32 v159, v71
	v_exp_f32_e32 v160, v72
	v_exp_f32_e32 v161, v73
	v_exp_f32_e32 v162, v74
	v_exp_f32_e32 v163, v75
	v_exp_f32_e32 v164, v76
	v_exp_f32_e32 v165, v77
	v_exp_f32_e32 v166, v78
	v_exp_f32_e32 v167, v79
	v_exp_f32_e32 v168, v80
	v_exp_f32_e32 v169, v81
	v_exp_f32_e32 v170, v82
	v_exp_f32_e32 v171, v83
	v_add_f32_e32 v249, v156, v157
	v_add_f32_e32 v250, v158, v159
	v_add_f32_e32 v249, v249, v160
	v_add_f32_e32 v250, v250, v161
	v_add_f32_e32 v249, v249, v162
	v_add_f32_e32 v250, v250, v163
	v_add_f32_e32 v249, v249, v164
	v_add_f32_e32 v250, v250, v165
	v_add_f32_e32 v249, v249, v166
	v_add_f32_e32 v250, v250, v167
	v_add_f32_e32 v249, v249, v168
	v_add_f32_e32 v250, v250, v169
	v_add_f32_e32 v249, v249, v170
	v_add_f32_e32 v250, v250, v171
	v_add_f32_e32 v249, v249, v250
	v_cvt_pk_bf16_f32 v156, v156, v157
	v_cvt_pk_bf16_f32 v157, v158, v159
	v_cvt_pk_bf16_f32 v158, v160, v161
	v_cvt_pk_bf16_f32 v159, v162, v163
	v_cvt_pk_bf16_f32 v160, v164, v165
	v_cvt_pk_bf16_f32 v161, v166, v167
	v_cvt_pk_bf16_f32 v162, v168, v169
	v_cvt_pk_bf16_f32 v163, v170, v171
	s_nop 1
	v_permlane32_swap_b32_e32 v156, v158
	v_permlane32_swap_b32_e32 v157, v159
	v_permlane32_swap_b32_e32 v160, v162
	v_permlane32_swap_b32_e32 v161, v163
	s_branch .Lsum_a1b1
.Lsub_a1b1:
	v_sub_f32_e32 v140, v84, v192
	v_sub_f32_e32 v141, v85, v192
	v_sub_f32_e32 v142, v86, v192
	v_sub_f32_e32 v143, v87, v192
	v_sub_f32_e32 v144, v88, v192
	v_sub_f32_e32 v145, v89, v192
	v_sub_f32_e32 v146, v90, v192
	v_sub_f32_e32 v147, v91, v192
	v_sub_f32_e32 v148, v92, v192
	v_sub_f32_e32 v149, v93, v192
	v_sub_f32_e32 v150, v94, v192
	v_sub_f32_e32 v151, v95, v192
	v_sub_f32_e32 v152, v96, v192
	v_sub_f32_e32 v153, v97, v192
	v_sub_f32_e32 v154, v98, v192
	v_sub_f32_e32 v155, v99, v192
	v_exp_f32_e32 v140, v140
	v_exp_f32_e32 v141, v141
	v_exp_f32_e32 v142, v142
	v_exp_f32_e32 v143, v143
	v_exp_f32_e32 v144, v144
	v_exp_f32_e32 v145, v145
	v_exp_f32_e32 v146, v146
	v_exp_f32_e32 v147, v147
	v_exp_f32_e32 v148, v148
	v_exp_f32_e32 v149, v149
	v_exp_f32_e32 v150, v150
	v_exp_f32_e32 v151, v151
	v_exp_f32_e32 v152, v152
	v_exp_f32_e32 v153, v153
	v_exp_f32_e32 v154, v154
	v_exp_f32_e32 v155, v155
	v_add_f32_e32 v248, v140, v141
	v_add_f32_e32 v250, v142, v143
	v_add_f32_e32 v248, v248, v144
	v_add_f32_e32 v250, v250, v145
	v_add_f32_e32 v248, v248, v146
	v_add_f32_e32 v250, v250, v147
	v_add_f32_e32 v248, v248, v148
	v_add_f32_e32 v250, v250, v149
	v_add_f32_e32 v248, v248, v150
	v_add_f32_e32 v250, v250, v151
	v_add_f32_e32 v248, v248, v152
	v_add_f32_e32 v250, v250, v153
	v_add_f32_e32 v248, v248, v154
	v_add_f32_e32 v250, v250, v155
	v_add_f32_e32 v248, v248, v250
	v_cvt_pk_bf16_f32 v140, v140, v141
	v_cvt_pk_bf16_f32 v141, v142, v143
	v_cvt_pk_bf16_f32 v142, v144, v145
	v_cvt_pk_bf16_f32 v143, v146, v147
	v_cvt_pk_bf16_f32 v144, v148, v149
	v_cvt_pk_bf16_f32 v145, v150, v151
	v_cvt_pk_bf16_f32 v146, v152, v153
	v_cvt_pk_bf16_f32 v147, v154, v155
	s_nop 1
	v_permlane32_swap_b32_e32 v140, v142
	v_permlane32_swap_b32_e32 v141, v143
	v_permlane32_swap_b32_e32 v144, v146
	v_permlane32_swap_b32_e32 v145, v147
	v_sub_f32_e32 v156, v68, v192
	v_sub_f32_e32 v157, v69, v192
	v_sub_f32_e32 v158, v70, v192
	v_sub_f32_e32 v159, v71, v192
	v_sub_f32_e32 v160, v72, v192
	v_sub_f32_e32 v161, v73, v192
	v_sub_f32_e32 v162, v74, v192
	v_sub_f32_e32 v163, v75, v192
	v_sub_f32_e32 v164, v76, v192
	v_sub_f32_e32 v165, v77, v192
	v_sub_f32_e32 v166, v78, v192
	v_sub_f32_e32 v167, v79, v192
	v_sub_f32_e32 v168, v80, v192
	v_sub_f32_e32 v169, v81, v192
	v_sub_f32_e32 v170, v82, v192
	v_sub_f32_e32 v171, v83, v192
	v_exp_f32_e32 v156, v156
	v_exp_f32_e32 v157, v157
	v_exp_f32_e32 v158, v158
	v_exp_f32_e32 v159, v159
	v_exp_f32_e32 v160, v160
	v_exp_f32_e32 v161, v161
	v_exp_f32_e32 v162, v162
	v_exp_f32_e32 v163, v163
	v_exp_f32_e32 v164, v164
	v_exp_f32_e32 v165, v165
	v_exp_f32_e32 v166, v166
	v_exp_f32_e32 v167, v167
	v_exp_f32_e32 v168, v168
	v_exp_f32_e32 v169, v169
	v_exp_f32_e32 v170, v170
	v_exp_f32_e32 v171, v171
	v_add_f32_e32 v249, v156, v157
	v_add_f32_e32 v250, v158, v159
	v_add_f32_e32 v249, v249, v160
	v_add_f32_e32 v250, v250, v161
	v_add_f32_e32 v249, v249, v162
	v_add_f32_e32 v250, v250, v163
	v_add_f32_e32 v249, v249, v164
	v_add_f32_e32 v250, v250, v165
	v_add_f32_e32 v249, v249, v166
	v_add_f32_e32 v250, v250, v167
	v_add_f32_e32 v249, v249, v168
	v_add_f32_e32 v250, v250, v169
	v_add_f32_e32 v249, v249, v170
	v_add_f32_e32 v250, v250, v171
	v_add_f32_e32 v249, v249, v250
	v_cvt_pk_bf16_f32 v156, v156, v157
	v_cvt_pk_bf16_f32 v157, v158, v159
	v_cvt_pk_bf16_f32 v158, v160, v161
	v_cvt_pk_bf16_f32 v159, v162, v163
	v_cvt_pk_bf16_f32 v160, v164, v165
	v_cvt_pk_bf16_f32 v161, v166, v167
	v_cvt_pk_bf16_f32 v162, v168, v169
	v_cvt_pk_bf16_f32 v163, v170, v171
	s_nop 1
	v_permlane32_swap_b32_e32 v156, v158
	v_permlane32_swap_b32_e32 v157, v159
	v_permlane32_swap_b32_e32 v160, v162
	v_permlane32_swap_b32_e32 v161, v163
.Lsum_a1b1:
	v_add_f32_e32 v248, v248, v249
	v_cmp_gt_f32_e32 vcc, 0x5f800000, v248
	s_cmp_eq_u64 vcc, exec
	s_cbranch_scc0 .Lfb_a1b1
	v_mov_b32_e32 v249, v248
	s_nop 1
	v_permlane32_swap_b32_e32 v248, v249
	v_add_f32_e32 v248, v248, v249
	v_add_f32_e32 v191, v248, v191
	v_mov_b32_e32 v193, v192
	s_waitcnt lgkmcnt(6)
	v_mfma_f32_32x32x16_bf16 v[52:67], v[208:211], v[140:143], v[52:67]
	ds_read_b64_tr_b16 v[208:209], v174 offset:16896
	ds_read_b64_tr_b16 v[210:211], v174 offset:18944
	s_waitcnt lgkmcnt(6)
	v_mfma_f32_32x32x16_bf16 v[52:67], v[212:215], v[144:147], v[52:67]
	ds_read_b64_tr_b16 v[212:213], v174 offset:20992
	ds_read_b64_tr_b16 v[214:215], v174 offset:23040
	s_waitcnt lgkmcnt(6)
	v_mfma_f32_32x32x16_bf16 v[52:67], v[216:219], v[156:159], v[52:67]
	ds_read_b64_tr_b16 v[216:217], v174 offset:25088
	ds_read_b64_tr_b16 v[218:219], v174 offset:27136
	s_waitcnt lgkmcnt(6)
	v_mfma_f32_32x32x16_bf16 v[52:67], v[220:223], v[160:163], v[52:67]
	ds_read_b64_tr_b16 v[220:221], v174 offset:29184
	ds_read_b64_tr_b16 v[222:223], v174 offset:31232
	s_waitcnt lgkmcnt(6)
	v_mfma_f32_32x32x16_bf16 v[36:51], v[208:211], v[140:143], v[36:51]
	ds_read_b64_tr_b16 v[208:209], v174 offset:17408
	ds_read_b64_tr_b16 v[210:211], v174 offset:19456
	s_waitcnt lgkmcnt(6)
	v_mfma_f32_32x32x16_bf16 v[36:51], v[212:215], v[144:147], v[36:51]
	ds_read_b64_tr_b16 v[212:213], v174 offset:21504
	ds_read_b64_tr_b16 v[214:215], v174 offset:23552
	s_waitcnt lgkmcnt(6)
	v_mfma_f32_32x32x16_bf16 v[36:51], v[216:219], v[156:159], v[36:51]
	ds_read_b64_tr_b16 v[216:217], v174 offset:25600
	ds_read_b64_tr_b16 v[218:219], v174 offset:27648
	s_waitcnt lgkmcnt(6)
	v_mfma_f32_32x32x16_bf16 v[36:51], v[220:223], v[160:163], v[36:51]
	ds_read_b64_tr_b16 v[220:221], v174 offset:29696
	ds_read_b64_tr_b16 v[222:223], v174 offset:31744
	s_waitcnt lgkmcnt(6)
	v_mfma_f32_32x32x16_bf16 v[20:35], v[208:211], v[140:143], v[20:35]
	ds_read_b64_tr_b16 v[208:209], v174 offset:17920
	ds_read_b64_tr_b16 v[210:211], v174 offset:19968
	s_waitcnt lgkmcnt(6)
	v_mfma_f32_32x32x16_bf16 v[20:35], v[212:215], v[144:147], v[20:35]
	ds_read_b64_tr_b16 v[212:213], v174 offset:22016
	ds_read_b64_tr_b16 v[214:215], v174 offset:24064
	s_waitcnt lgkmcnt(6)
	v_mfma_f32_32x32x16_bf16 v[20:35], v[216:219], v[156:159], v[20:35]
	ds_read_b64_tr_b16 v[216:217], v174 offset:26112
	ds_read_b64_tr_b16 v[218:219], v174 offset:28160
	s_waitcnt lgkmcnt(6)
	v_mfma_f32_32x32x16_bf16 v[20:35], v[220:223], v[160:163], v[20:35]
	ds_read_b64_tr_b16 v[220:221], v174 offset:30208
	ds_read_b64_tr_b16 v[222:223], v174 offset:32256
	s_waitcnt lgkmcnt(6)
	v_mfma_f32_32x32x16_bf16 v[4:19], v[208:211], v[140:143], v[4:19]
	s_waitcnt lgkmcnt(4)
	v_mfma_f32_32x32x16_bf16 v[4:19], v[212:215], v[144:147], v[4:19]
	s_waitcnt lgkmcnt(2)
	v_mfma_f32_32x32x16_bf16 v[4:19], v[216:219], v[156:159], v[4:19]
	s_waitcnt lgkmcnt(0)
	v_mfma_f32_32x32x16_bf16 v[4:19], v[220:223], v[160:163], v[4:19]
	s_setprio 0
	s_branch .Ltail2_a1b1
